# stack10 + attention tile loop row-sum chain: six v_pk_add_f32 split into scalar v_add_f32 pairs (bit-identical)
# speedup vs baseline: 1.0020x; 1.0020x over previous
.LBB0_436:
	v_add_f32_e32 v100, v68, v84
	v_add_f32_e32 v100, 0, v100
	v_add_f32_e32 v101, v69, v85
	v_add_f32_e32 v100, v101, v100
	v_add_f32_e32 v101, v70, v86
	v_add_f32_e32 v100, v101, v100
	v_add_f32_e32 v101, v71, v87
	v_add_f32_e32 v112, v101, v100
	v_add_f32_e32 v110, v72, v88
	v_add_f32_e32 v111, v73, v89
	v_add_f32_e32 v108, v74, v90
	v_add_f32_e32 v109, v75, v91
	v_add_f32_e32 v110, v110, v112
	v_add_f32_e32 v110, v111, v110
	v_add_f32_e32 v108, v108, v110
	v_add_f32_e32 v106, v76, v92
	v_add_f32_e32 v107, v77, v93
	v_add_f32_e32 v108, v109, v108
	v_add_f32_e32 v106, v106, v108
	v_add_f32_e32 v104, v78, v94
	v_add_f32_e32 v105, v79, v95
	v_add_f32_e32 v106, v107, v106
	v_add_f32_e32 v104, v104, v106
	v_add_f32_e32 v102, v80, v96
	v_add_f32_e32 v103, v81, v97
	v_add_f32_e32 v104, v105, v104
	v_add_f32_e32 v102, v102, v104
	v_add_f32_e32 v100, v82, v98
	v_add_f32_e32 v101, v83, v99
	v_add_f32_e32 v102, v103, v102
	v_add_f32_e32 v100, v100, v102
	v_add_f32_e32 v152, v101, v100
	s_mov_b32 s0, 0x46000000
	v_cmp_nge_f32_e32 vcc, s0, v152
	s_cbranch_vccz .LBB0_438
	v_max_f32_e32 v100, v69, v69
	v_max_f32_e32 v101, v68, v68
	v_max_f32_e32 v100, v101, v100
	v_max_f32_e32 v101, v71, v71
	v_max_f32_e32 v102, v70, v70
	v_max_f32_e32 v101, v102, v101
	v_max_f32_e32 v102, v75, v75
	v_max_f32_e32 v103, v74, v74
	v_max_f32_e32 v102, v103, v102
	v_max3_f32 v102, v72, v73, v102
	v_max3_f32 v100, v100, v101, v102
	v_max_f32_e32 v101, v77, v77
	v_max_f32_e32 v102, v76, v76
	v_max_f32_e32 v101, v102, v101
	v_max_f32_e32 v102, v79, v79
	v_max_f32_e32 v103, v78, v78
	v_max_f32_e32 v102, v103, v102
	v_max_f32_e32 v103, v83, v83
	v_max_f32_e32 v104, v82, v82
	v_max_f32_e32 v103, v104, v103
	v_max3_f32 v103, v80, v81, v103
	v_max3_f32 v101, v101, v102, v103
	v_max_f32_e32 v102, v87, v87
	v_max_f32_e32 v103, v86, v86
	v_max_f32_e32 v102, v103, v102
	v_max_f32_e32 v103, v91, v91
	v_max_f32_e32 v104, v90, v90
	v_max_f32_e32 v103, v104, v103
	v_max_f32_e32 v104, v93, v93
	v_max_f32_e32 v105, v92, v92
	v_max_f32_e32 v104, v105, v104
	v_max_f32_e32 v105, v95, v95
	v_max_f32_e32 v106, v94, v94
	v_max_f32_e32 v105, v106, v105
	v_max_f32_e32 v106, v99, v99
	v_max_f32_e32 v107, v98, v98
	v_max_f32_e32 v106, v107, v106
	v_max3_f32 v106, v96, v97, v106
	v_max3_f32 v102, v84, v85, v102
	v_max3_f32 v103, v88, v89, v103
	v_max3_f32 v104, v104, v105, v106
	v_max3_f32 v102, v102, v103, v104
	v_max3_f32 v100, v100, v101, v102
	v_mov_b32_e32 v101, v100
	s_nop 1
	v_permlane32_swap_b32 v101, v100
	s_nop 1
	s_nop 0
	v_max3_f32 v101, v101, v100, 1.0
	v_rcp_f32_e32 v100, v101
	s_nop 0
	v_pk_mul_f32 v[66:67], v[66:67], v[100:101] op_sel_hi:[1,0]
	v_pk_mul_f32 v[64:65], v[64:65], v[100:101] op_sel_hi:[1,0]
	v_pk_mul_f32 v[62:63], v[62:63], v[100:101] op_sel_hi:[1,0]
	v_pk_mul_f32 v[60:61], v[60:61], v[100:101] op_sel_hi:[1,0]
	v_pk_mul_f32 v[58:59], v[58:59], v[100:101] op_sel_hi:[1,0]
	v_pk_mul_f32 v[56:57], v[56:57], v[100:101] op_sel_hi:[1,0]
	v_pk_mul_f32 v[54:55], v[54:55], v[100:101] op_sel_hi:[1,0]
	v_pk_mul_f32 v[52:53], v[52:53], v[100:101] op_sel_hi:[1,0]
	v_pk_mul_f32 v[50:51], v[50:51], v[100:101] op_sel_hi:[1,0]
	v_pk_mul_f32 v[48:49], v[48:49], v[100:101] op_sel_hi:[1,0]
	v_pk_mul_f32 v[46:47], v[46:47], v[100:101] op_sel_hi:[1,0]
	v_pk_mul_f32 v[44:45], v[44:45], v[100:101] op_sel_hi:[1,0]
	v_pk_mul_f32 v[42:43], v[42:43], v[100:101] op_sel_hi:[1,0]
	v_pk_mul_f32 v[40:41], v[40:41], v[100:101] op_sel_hi:[1,0]
	v_pk_mul_f32 v[38:39], v[38:39], v[100:101] op_sel_hi:[1,0]
	v_pk_mul_f32 v[36:37], v[36:37], v[100:101] op_sel_hi:[1,0]
	v_pk_mul_f32 v[34:35], v[34:35], v[100:101] op_sel_hi:[1,0]
	v_pk_mul_f32 v[32:33], v[32:33], v[100:101] op_sel_hi:[1,0]
	v_pk_mul_f32 v[30:31], v[30:31], v[100:101] op_sel_hi:[1,0]
	v_pk_mul_f32 v[28:29], v[28:29], v[100:101] op_sel_hi:[1,0]
	v_pk_mul_f32 v[26:27], v[26:27], v[100:101] op_sel_hi:[1,0]
	v_pk_mul_f32 v[24:25], v[24:25], v[100:101] op_sel_hi:[1,0]
	v_pk_mul_f32 v[22:23], v[22:23], v[100:101] op_sel_hi:[1,0]
	v_pk_mul_f32 v[20:21], v[20:21], v[100:101] op_sel_hi:[1,0]
	v_pk_mul_f32 v[18:19], v[18:19], v[100:101] op_sel_hi:[1,0]
	v_pk_mul_f32 v[16:17], v[16:17], v[100:101] op_sel_hi:[1,0]
	v_pk_mul_f32 v[14:15], v[14:15], v[100:101] op_sel_hi:[1,0]
	v_pk_mul_f32 v[12:13], v[12:13], v[100:101] op_sel_hi:[1,0]
	v_pk_mul_f32 v[10:11], v[10:11], v[100:101] op_sel_hi:[1,0]
	v_pk_mul_f32 v[8:9], v[8:9], v[100:101] op_sel_hi:[1,0]
	v_pk_mul_f32 v[6:7], v[6:7], v[100:101] op_sel_hi:[1,0]
	v_pk_mul_f32 v[4:5], v[4:5], v[100:101] op_sel_hi:[1,0]
	v_log_f32_e32 v101, v101
	s_nop 0
	v_pk_mul_f32 v[82:83], v[82:83], v[100:101] op_sel_hi:[1,0]
	v_pk_mul_f32 v[80:81], v[80:81], v[100:101] op_sel_hi:[1,0]
	v_pk_mul_f32 v[78:79], v[78:79], v[100:101] op_sel_hi:[1,0]
	v_pk_mul_f32 v[76:77], v[76:77], v[100:101] op_sel_hi:[1,0]
	v_pk_mul_f32 v[74:75], v[74:75], v[100:101] op_sel_hi:[1,0]
	v_pk_mul_f32 v[72:73], v[72:73], v[100:101] op_sel_hi:[1,0]
	v_pk_mul_f32 v[70:71], v[70:71], v[100:101] op_sel_hi:[1,0]
	v_pk_mul_f32 v[68:69], v[68:69], v[100:101] op_sel_hi:[1,0]
	v_pk_mul_f32 v[98:99], v[98:99], v[100:101] op_sel_hi:[1,0]
	v_pk_mul_f32 v[96:97], v[96:97], v[100:101] op_sel_hi:[1,0]
	v_pk_mul_f32 v[94:95], v[94:95], v[100:101] op_sel_hi:[1,0]
	v_pk_mul_f32 v[92:93], v[92:93], v[100:101] op_sel_hi:[1,0]
	v_pk_mul_f32 v[90:91], v[90:91], v[100:101] op_sel_hi:[1,0]
	v_pk_mul_f32 v[88:89], v[88:89], v[100:101] op_sel_hi:[1,0]
	v_pk_mul_f32 v[86:87], v[86:87], v[100:101] op_sel_hi:[1,0]
	v_pk_mul_f32 v[84:85], v[84:85], v[100:101] op_sel_hi:[1,0]
	v_add_f32_e32 v167, v167, v101
	v_pk_mul_f32 v[152:153], v[152:153], v[100:101] op_sel_hi:[1,0]
